# baseline (speedup 1.0000x reference)
.Lw2k_w1:
	s_barrier
	ds_read_b128 v[162:165], v178
	ds_read_b128 v[166:169], v178 offset:4096
	ds_read_b128 v[170:173], v174 offset:6144
	ds_read_b128 v[174:177], v174 offset:2048
	ds_read_b128 v[178:181], v178 offset:8192
	ds_read_b64_tr_b16 v[182:183], v200 offset:0
	ds_read_b64_tr_b16 v[184:185], v200 offset:0x400
	ds_read_b64_tr_b16 v[186:187], v201 offset:0
	ds_read_b64_tr_b16 v[188:189], v201 offset:0x400
	ds_read_b64_tr_b16 v[190:191], v202 offset:0
	ds_read_b64_tr_b16 v[192:193], v202 offset:0x400
	ds_read_b64_tr_b16 v[194:195], v203 offset:0
	ds_read_b64_tr_b16 v[196:197], v203 offset:0x400
	global_load_lds_dwordx4 v[120:121], off sc1
	v_lshl_add_u64 v[198:199], v[120:121], 0, s[16:17]
	s_mov_b32 m0, s14
	v_readfirstlane_b32 s14, v205
	v_add_u32_e32 v205, 0x8000, v204
	global_load_lds_dwordx4 v[198:199], off sc1
	v_lshl_add_u64 v[198:199], v[120:121], 0, s[18:19]
	s_mov_b32 m0, s14
	v_readfirstlane_b32 s14, v205
	global_load_lds_dwordx4 v[198:199], off sc1
	v_lshl_add_u64 v[198:199], v[120:121], 0, s[20:21]
	s_mov_b32 m0, s14
	s_nop 0
	global_load_lds_dwordx4 v[198:199], off sc1
	s_waitcnt lgkmcnt(0)
	s_waitcnt lgkmcnt(0)
	v_mfma_f32_16x16x32_f16 v[92:95], v[182:185], v[162:165], v[92:95]
	v_mfma_f32_16x16x32_f16 v[88:91], v[186:189], v[162:165], v[88:91]
	v_mfma_f32_16x16x32_f16 v[84:87], v[190:193], v[162:165], v[84:87]
	v_mfma_f32_16x16x32_f16 v[80:83], v[194:197], v[162:165], v[80:83]
	v_mfma_f32_16x16x32_f16 v[76:79], v[182:185], v[174:177], v[76:79]
	v_mfma_f32_16x16x32_f16 v[72:75], v[186:189], v[174:177], v[72:75]
	v_mfma_f32_16x16x32_f16 v[68:71], v[190:193], v[174:177], v[68:71]
	v_mfma_f32_16x16x32_f16 v[64:67], v[194:197], v[174:177], v[64:67]
	v_mfma_f32_16x16x32_f16 v[60:63], v[182:185], v[166:169], v[60:63]
	v_mfma_f32_16x16x32_f16 v[56:59], v[186:189], v[166:169], v[56:59]
	v_mfma_f32_16x16x32_f16 v[52:55], v[190:193], v[166:169], v[52:55]
	v_mfma_f32_16x16x32_f16 v[48:51], v[194:197], v[166:169], v[48:51]
	v_mfma_f32_16x16x32_f16 v[44:47], v[182:185], v[170:173], v[44:47]
	v_mfma_f32_16x16x32_f16 v[40:43], v[186:189], v[170:173], v[40:43]
	v_mfma_f32_16x16x32_f16 v[36:39], v[190:193], v[170:173], v[36:39]
	v_mfma_f32_16x16x32_f16 v[32:35], v[194:197], v[170:173], v[32:35]
	v_mfma_f32_16x16x32_f16 v[28:31], v[182:185], v[178:181], v[28:31]
	v_mfma_f32_16x16x32_f16 v[24:27], v[186:189], v[178:181], v[24:27]
	v_mfma_f32_16x16x32_f16 v[20:23], v[190:193], v[178:181], v[20:23]
	v_mfma_f32_16x16x32_f16 v[16:19], v[194:197], v[178:181], v[16:19]
	v_add_u32_e32 v178, v161, v158
	v_add_u32_e32 v161, v161, v157
	ds_read_b128 v[162:165], v178
	ds_read_b128 v[166:169], v178 offset:4096
	ds_read_b128 v[170:173], v161 offset:6144
	ds_read_b128 v[174:177], v161 offset:2048
	ds_read_b128 v[178:181], v178 offset:8192
	v_readfirstlane_b32 s14, v204
	v_add_u32_e32 v161, 0x1000, v204
	v_lshl_add_u64 v[198:199], v[112:113], 0, s[0:1]
	s_mov_b32 m0, s14
	v_readfirstlane_b32 s14, v161
	v_add_u32_e32 v161, 0x2000, v204
	ds_read_b64_tr_b16 v[182:183], v200 offset:0x2000
	ds_read_b64_tr_b16 v[184:185], v200 offset:0x2400
	ds_read_b64_tr_b16 v[186:187], v201 offset:0x2000
	ds_read_b64_tr_b16 v[188:189], v201 offset:0x2400
	ds_read_b64_tr_b16 v[190:191], v202 offset:0x2000
	ds_read_b64_tr_b16 v[192:193], v202 offset:0x2400
	ds_read_b64_tr_b16 v[194:195], v203 offset:0x2000
	ds_read_b64_tr_b16 v[196:197], v203 offset:0x2400
	global_load_lds_dwordx4 v[198:199], off sc1
	v_lshl_add_u64 v[198:199], v[114:115], 0, s[0:1]
	s_mov_b32 m0, s14
	v_readfirstlane_b32 s14, v161
	v_add_u32_e32 v161, 0x3000, v204
	global_load_lds_dwordx4 v[198:199], off sc1
	v_lshl_add_u64 v[198:199], v[116:117], 0, s[0:1]
	s_mov_b32 m0, s14
	v_readfirstlane_b32 s14, v161
	v_add_u32_e32 v161, 0x4000, v204
	global_load_lds_dwordx4 v[198:199], off sc1
	v_lshl_add_u64 v[198:199], v[118:119], 0, s[0:1]
	s_mov_b32 m0, s14
	v_readfirstlane_b32 s14, v161
	global_load_lds_dwordx4 v[198:199], off sc1
	v_lshl_add_u64 v[198:199], v[122:123], 0, s[0:1]
	s_mov_b32 m0, s14
	s_nop 0
	global_load_lds_dwordx4 v[198:199], off sc1
	s_waitcnt lgkmcnt(0)
	s_waitcnt lgkmcnt(0)
	v_mfma_f32_16x16x32_f16 v[92:95], v[182:185], v[162:165], v[92:95]
	v_mfma_f32_16x16x32_f16 v[88:91], v[186:189], v[162:165], v[88:91]
	v_mfma_f32_16x16x32_f16 v[84:87], v[190:193], v[162:165], v[84:87]
	v_mfma_f32_16x16x32_f16 v[80:83], v[194:197], v[162:165], v[80:83]
	v_mfma_f32_16x16x32_f16 v[76:79], v[182:185], v[174:177], v[76:79]
	v_mfma_f32_16x16x32_f16 v[72:75], v[186:189], v[174:177], v[72:75]
	v_mfma_f32_16x16x32_f16 v[68:71], v[190:193], v[174:177], v[68:71]
	v_mfma_f32_16x16x32_f16 v[64:67], v[194:197], v[174:177], v[64:67]
	v_mfma_f32_16x16x32_f16 v[60:63], v[182:185], v[166:169], v[60:63]
	v_mfma_f32_16x16x32_f16 v[56:59], v[186:189], v[166:169], v[56:59]
	v_mfma_f32_16x16x32_f16 v[52:55], v[190:193], v[166:169], v[52:55]
	v_mfma_f32_16x16x32_f16 v[48:51], v[194:197], v[166:169], v[48:51]
	v_mfma_f32_16x16x32_f16 v[44:47], v[182:185], v[170:173], v[44:47]
	v_mfma_f32_16x16x32_f16 v[40:43], v[186:189], v[170:173], v[40:43]
	v_mfma_f32_16x16x32_f16 v[36:39], v[190:193], v[170:173], v[36:39]
	v_mfma_f32_16x16x32_f16 v[32:35], v[194:197], v[170:173], v[32:35]
	v_mfma_f32_16x16x32_f16 v[28:31], v[182:185], v[178:181], v[28:31]
	v_mfma_f32_16x16x32_f16 v[24:27], v[186:189], v[178:181], v[24:27]
	v_mfma_f32_16x16x32_f16 v[20:23], v[190:193], v[178:181], v[20:23]
	v_mfma_f32_16x16x32_f16 v[16:19], v[194:197], v[178:181], v[16:19]
	s_cmp_eq_u32 s97, 0
	s_cbranch_scc1 .Lw2k_noc
	s_waitcnt vmcnt(9)
	v_cvt_pk_f16_f32 v208, v208, v209
	v_cvt_pk_f16_f32 v209, v210, v211
	v_cvt_pk_f16_f32 v210, v212, v213
	v_cvt_pk_f16_f32 v211, v214, v215
	global_store_dwordx2 v217, v[208:209], s[94:95]
	global_store_dwordx2 v217, v[210:211], s[94:95] offset:512
	s_add_u32 s94, s94, 0x200000
	s_addc_u32 s95, s95, 0
	s_mov_b32 s97, 0
